# instruction selection in the per-step staging issue: the +0x8000 of the pair's second K block is folded into the scalar base (two SALU) instead of a VALU carry pair with its wait state
# baseline (speedup 1.0000x reference)
; __device__ __forceinline__ void stage_load(Stage& s, const unsigned char* kg, size_t kstride, const unsigned char* vg, size_t vstride, int tid, bool hasv) {
;     const int row = tid >> 3, ch = tid & 7;
;     s.k = *(const u32x4*)(kg + (size_t)row * kstride + ch * 16);
;     if (hasv) s.v = *(const u32x4*)(vg + (size_t)row * vstride + ch * 16);
; }
.Lbm_jA1:
	s_cmp_ge_i32 s75, s26
	s_cbranch_scc1 .Lbm_back
	s_add_u32 s12, s64, 0x10000
	s_addc_u32 s13, s65, 0
	s_add_u32 s14, s62, 0x100
	s_addc_u32 s15, s63, 0
	v_lshl_add_u64 v[78:79], s[14:15], 0, v[162:163]
	v_lshl_add_u64 v[80:81], s[12:13], 0, v[156:157]
	s_add_u32 s12, s12, 0x8000
	s_addc_u32 s13, s13, 0
	v_lshl_add_u64 v[254:255], s[14:15], 0, v[168:169]
	v_lshl_add_u64 v[78:79], v[78:79], 0, v[160:161]
	v_lshl_add_u64 v[80:81], v[80:81], 0, v[160:161]
	v_lshl_add_u64 v[82:83], s[12:13], 0, v[166:167]
	global_load_dwordx4 v[22:25], v[78:79], off
	global_load_dwordx4 v[26:29], v[80:81], off
	global_load_dwordx4 v[30:33], v[82:83], off
	global_load_dwordx4 v[34:37], v[254:255], off offset:128
	s_mov_b32 s99, 1
	s_cmp_gt_i32 s75, s10
	s_cbranch_scc1 .Lbm_back
	s_add_u32 s12, s64, 0x20000
	s_addc_u32 s13, s65, 0
	s_add_u32 s14, s62, 0x200
	s_addc_u32 s15, s63, 0
	v_lshl_add_u64 v[78:79], s[14:15], 0, v[162:163]
	v_lshl_add_u64 v[80:81], s[12:13], 0, v[156:157]
	s_add_u32 s12, s12, 0x8000
	s_addc_u32 s13, s13, 0
	v_lshl_add_u64 v[254:255], s[14:15], 0, v[168:169]
	v_lshl_add_u64 v[78:79], v[78:79], 0, v[160:161]
	v_lshl_add_u64 v[80:81], v[80:81], 0, v[160:161]
	v_lshl_add_u64 v[82:83], s[12:13], 0, v[166:167]
	global_load_dwordx4 v[6:9], v[78:79], off
	global_load_dwordx4 v[10:13], v[80:81], off
	global_load_dwordx4 v[14:17], v[82:83], off
	global_load_dwordx4 v[18:21], v[254:255], off offset:128
	s_mov_b32 s99, 2
	s_mov_b32 s101, 8
	s_branch .Lbm_back
.Lbm_jA2:
	s_mov_b32 s99, 4
	s_mov_b32 s101, 0
	s_cmp_gt_i32 s75, s10
	s_cbranch_scc1 .Lbm_back
	s_add_u32 s12, s64, 0x20000
	s_addc_u32 s13, s65, 0
	s_add_u32 s14, s62, 0x200
	s_addc_u32 s15, s63, 0
	v_lshl_add_u64 v[78:79], s[14:15], 0, v[162:163]
	v_lshl_add_u64 v[80:81], s[12:13], 0, v[156:157]
	s_add_u32 s12, s12, 0x8000
	s_addc_u32 s13, s13, 0
	v_lshl_add_u64 v[254:255], s[14:15], 0, v[168:169]
	v_lshl_add_u64 v[78:79], v[78:79], 0, v[160:161]
	v_lshl_add_u64 v[80:81], v[80:81], 0, v[160:161]
	v_lshl_add_u64 v[82:83], s[12:13], 0, v[166:167]
	global_load_dwordx4 v[22:25], v[78:79], off
	global_load_dwordx4 v[26:29], v[80:81], off
	global_load_dwordx4 v[30:33], v[82:83], off
	global_load_dwordx4 v[34:37], v[254:255], off offset:128
	s_mov_b32 s99, 3
	s_mov_b32 s101, 4
	s_branch .Lbm_back

; __device__ __forceinline__ void stage_load(Stage& s, const unsigned char* kg, size_t kstride, const unsigned char* vg, size_t vstride, int tid, bool hasv) {
;     const int row = tid >> 3, ch = tid & 7;
;     s.k = *(const u32x4*)(kg + (size_t)row * kstride + ch * 16);
;     if (hasv) s.v = *(const u32x4*)(vg + (size_t)row * vstride + ch * 16);
.Lbm_jB1:
	s_cmp_ge_i32 s75, s26
	s_cbranch_scc1 .Lbm_back
	s_add_u32 s12, s64, 0x10000
	s_addc_u32 s13, s65, 0
	s_add_u32 s14, s62, 0x100
	s_addc_u32 s15, s63, 0
	v_lshl_add_u64 v[78:79], s[14:15], 0, v[162:163]
	v_lshl_add_u64 v[80:81], s[12:13], 0, v[156:157]
	s_add_u32 s12, s12, 0x8000
	s_addc_u32 s13, s13, 0
	v_lshl_add_u64 v[254:255], s[14:15], 0, v[168:169]
	v_lshl_add_u64 v[78:79], v[78:79], 0, v[160:161]
	v_lshl_add_u64 v[80:81], v[80:81], 0, v[160:161]
	v_lshl_add_u64 v[82:83], s[12:13], 0, v[166:167]
	global_load_dwordx4 v[22:25], v[78:79], off
	global_load_dwordx4 v[26:29], v[80:81], off
	global_load_dwordx4 v[30:33], v[82:83], off
	global_load_dwordx4 v[34:37], v[254:255], off offset:128
	s_mov_b32 s99, 1
	s_branch .Lbm_back
.Lbm_jB3:
	s_mov_b32 s99, 1
	s_mov_b32 s101, 0
	s_cmp_gt_i32 s75, s10
	s_cbranch_scc1 .Lbm_back
	s_add_u32 s12, s64, 0x20000
	s_addc_u32 s13, s65, 0
	s_add_u32 s14, s62, 0x200
	s_addc_u32 s15, s63, 0
	v_lshl_add_u64 v[78:79], s[14:15], 0, v[162:163]
	v_lshl_add_u64 v[80:81], s[12:13], 0, v[156:157]
	s_add_u32 s12, s12, 0x8000
	s_addc_u32 s13, s13, 0
	v_lshl_add_u64 v[254:255], s[14:15], 0, v[168:169]
	v_lshl_add_u64 v[78:79], v[78:79], 0, v[160:161]
	v_lshl_add_u64 v[80:81], v[80:81], 0, v[160:161]
	v_lshl_add_u64 v[82:83], s[12:13], 0, v[166:167]
	global_load_dwordx4 v[6:9], v[78:79], off
	global_load_dwordx4 v[10:13], v[80:81], off
	global_load_dwordx4 v[14:17], v[82:83], off
	global_load_dwordx4 v[18:21], v[254:255], off offset:128
	s_mov_b32 s99, 2
	s_mov_b32 s101, 4
	s_branch .Lbm_back
